# P1 gate epilogue rewritten: -log2e folded into row scale, packed add/fma, SDWA byte inserts (25 pct fewer VALU cycles); on top of z-gate L2 touch
# baseline (speedup 1.0000x reference)
;     template <int ACT, int AUX> __device__ __forceinline__ void run(const f32x4 (&acc)[2][2][4][2], const Unit& uu, int wr, int wc, int fr, int fq) const {
;     ...
;         for (int i = 0; i < 8; ++i) rsv[i] = ss[row0 + (i >> 2) * HALF + (i & 3) * 16];
;         asm volatile("" ::: "memory");
; #pragma unroll
;         for (int i = 0; i < 8; ++i) rsv[i] = __builtin_amdgcn_rsqf(rsv[i] * (1.0f / cfg::DM) + cfg::RMS_EPS);
;         float cs[2][8]; float mx[2][2];
;         if (AUX == 1) {
; #pragma unroll
;             for (int i = 0; i < 16; ++i) cs[i >> 3][i & 7] = 0.f; }
;         if (AUX == 2) { mx[0][0] = mx[0][1] = mx[1][0] = mx[1][1] = 0.f; }
; #pragma unroll
;         for (int ai = 0; ai < 2; ++ai)
; #pragma unroll
;             for (int m = 0; m < 4; ++m) { const int r = row0 + ai * HALF + m * 16; const float rs = rsv[ai * 4 + m];
;                 bf16_t* rowp = O + (size_t)r * cfg::NC + col0; float s1 = 0.f, s2 = 0.f;
; #pragma unroll
;                 for (int bj = 0; bj < 2; ++bj) { f32x4 v0 = acc[ai][bj][m][0] * rs, v1 = acc[ai][bj][m][1] * rs;
; #pragma unroll
;                     for (int j = 0; j < 4; ++j) { v0[j] = act_f<ACT>(v0[j]); v1[j] = act_f<ACT>(v1[j]); }
;                     if (AUX == 4) {
;                         unsigned q[8];
; #pragma unroll
;                         for (int j = 0; j < 4; ++j) { q[j] = (unsigned)fminf(fmaxf(fmaf(v0[j], 255.0f, 0.5f), 1.0f), 255.0f); q[4 + j] = (unsigned)fminf(fmaxf(fmaf(v1[j], 255.0f, 0.5f), 1.0f), 255.0f); }
;                         u32x2 w8; w8.x = q[0] | (q[1] << 8) | (q[2] << 16) | (q[3] << 24); w8.y = q[4] | (q[5] << 8) | (q[6] << 16) | (q[7] << 24);
;                         __builtin_nontemporal_store(w8, (u32x2*)(g8 + ((size_t)((u.pn - 52) >> 4) * cfg::MT + r) * cfg::DM + ((u.pn - 52) & 15) * BM + wc * 32 + 8 * fq + bj * HALF));
.LBB0_157:
	v_lshl_add_u32 v156, s2, 8, v1
	v_ashrrev_i32_e32 v157, 31, v156
	s_waitcnt lgkmcnt(0)
	v_lshl_add_u64 v[146:147], v[156:157], 2, s[22:23]
	global_load_dword v151, v[146:147], off
	global_load_dword v153, v[146:147], off offset:64
	global_load_dword v155, v[146:147], off offset:128
	global_load_dword v157, v[146:147], off offset:192
	global_load_dword v159, v[146:147], off offset:512
	global_load_dword v154, v[146:147], off offset:576
	global_load_dword v156, v[146:147], off offset:640
	global_load_dword v158, v[146:147], off offset:704
	s_lshl_b32 s100, s2, 20
	s_sub_i32 s12, s1, 52
	s_lshr_b32 s2, s12, 4
	s_lshl_b32 s39, s12, 8
	s_lshl_b64 s[12:13], s[2:3], 25
	s_and_b32 s2, s39, 0xf00
	s_add_u32 s12, s63, s12
	s_addc_u32 s13, s64, s13
	s_lshl_b32 s101, s2, 8
	s_add_i32 s100, s100, s101
	s_lshl_b32 s101, s58, 3
	s_add_i32 s100, s100, s101
	s_addk_i32 s100, 0x1000
	s_add_u32 s100, s12, s100
	s_addc_u32 s101, s13, 0
	v_mbcnt_lo_u32_b32 v148, -1, 0
	v_mbcnt_hi_u32_b32 v148, -1, v148
	v_lshlrev_b32_e32 v148, 3, v148
	v_mov_b32_e32 v149, 0
	v_lshl_add_u64 v[148:149], s[100:101], 0, v[148:149]
	s_mov_b32 s39, 0x437f0000
	v_mov_b32_e32 v146, 1.0
	v_mov_b32_e32 v150, 0x437f0000
	v_mov_b32_e32 v152, 0.5
	s_waitcnt vmcnt(0)
	v_fmamk_f32 v164, v151, 0x39800000, v221
	v_rsq_f32_e32 v164, v164
	v_fmamk_f32 v162, v153, 0x39800000, v221
	v_rsq_f32_e32 v162, v162
	v_mul_f32_e32 v164, 0xbfb8aa3b, v164
	v_mul_f32_e32 v162, 0xbfb8aa3b, v162
	v_pk_mul_f32 v[128:129], v[128:129], v[164:165] op_sel_hi:[1,0]
	v_pk_mul_f32 v[130:131], v[130:131], v[164:165] op_sel_hi:[1,0]
	v_pk_mul_f32 v[124:125], v[124:125], v[164:165] op_sel_hi:[1,0]
	v_pk_mul_f32 v[126:127], v[126:127], v[164:165] op_sel_hi:[1,0]
	v_pk_mul_f32 v[120:121], v[120:121], v[164:165] op_sel_hi:[1,0]
	v_pk_mul_f32 v[122:123], v[122:123], v[164:165] op_sel_hi:[1,0]
	v_pk_mul_f32 v[116:117], v[116:117], v[164:165] op_sel_hi:[1,0]
	v_pk_mul_f32 v[118:119], v[118:119], v[164:165] op_sel_hi:[1,0]
	v_fmamk_f32 v160, v155, 0x39800000, v221
	v_rsq_f32_e32 v160, v160
	v_exp_f32_e32 v128, v128
	v_exp_f32_e32 v129, v129
	v_exp_f32_e32 v130, v130
	v_exp_f32_e32 v131, v131
	v_mul_f32_e32 v160, 0xbfb8aa3b, v160
	v_exp_f32_e32 v124, v124
	v_exp_f32_e32 v125, v125
	v_exp_f32_e32 v126, v126
	v_exp_f32_e32 v127, v127
	v_exp_f32_e32 v120, v120
	v_exp_f32_e32 v121, v121
	v_exp_f32_e32 v122, v122
	v_exp_f32_e32 v123, v123
	v_exp_f32_e32 v116, v116
	v_exp_f32_e32 v117, v117
	v_exp_f32_e32 v118, v118
	v_exp_f32_e32 v119, v119
	v_pk_add_f32 v[128:129], v[128:129], v[146:147] op_sel_hi:[1,0]
	v_pk_add_f32 v[130:131], v[130:131], v[146:147] op_sel_hi:[1,0]
	v_pk_add_f32 v[124:125], v[124:125], v[146:147] op_sel_hi:[1,0]
	v_pk_add_f32 v[126:127], v[126:127], v[146:147] op_sel_hi:[1,0]
	v_pk_add_f32 v[120:121], v[120:121], v[146:147] op_sel_hi:[1,0]
	v_pk_add_f32 v[122:123], v[122:123], v[146:147] op_sel_hi:[1,0]
	v_pk_add_f32 v[116:117], v[116:117], v[146:147] op_sel_hi:[1,0]
	v_pk_add_f32 v[118:119], v[118:119], v[146:147] op_sel_hi:[1,0]
	v_rcp_f32_e32 v128, v128
	v_rcp_f32_e32 v129, v129
	v_rcp_f32_e32 v130, v130
	v_rcp_f32_e32 v131, v131
	v_rcp_f32_e32 v124, v124
	v_rcp_f32_e32 v125, v125
	v_rcp_f32_e32 v126, v126
	v_rcp_f32_e32 v127, v127
	v_rcp_f32_e32 v120, v120
	v_rcp_f32_e32 v121, v121
	v_rcp_f32_e32 v122, v122
	v_rcp_f32_e32 v123, v123
	v_rcp_f32_e32 v116, v116
	v_rcp_f32_e32 v117, v117
	v_rcp_f32_e32 v118, v118
	v_rcp_f32_e32 v119, v119
	v_pk_fma_f32 v[128:129], v[128:129], v[150:151], v[152:153] op_sel_hi:[1,0,0]
	v_pk_fma_f32 v[130:131], v[130:131], v[150:151], v[152:153] op_sel_hi:[1,0,0]
	v_pk_fma_f32 v[124:125], v[124:125], v[150:151], v[152:153] op_sel_hi:[1,0,0]
	v_pk_fma_f32 v[126:127], v[126:127], v[150:151], v[152:153] op_sel_hi:[1,0,0]
	v_pk_fma_f32 v[120:121], v[120:121], v[150:151], v[152:153] op_sel_hi:[1,0,0]
	v_pk_fma_f32 v[122:123], v[122:123], v[150:151], v[152:153] op_sel_hi:[1,0,0]
	v_pk_fma_f32 v[116:117], v[116:117], v[150:151], v[152:153] op_sel_hi:[1,0,0]
	v_pk_fma_f32 v[118:119], v[118:119], v[150:151], v[152:153] op_sel_hi:[1,0,0]
	v_med3_f32 v128, v128, 1.0, v231
	v_med3_f32 v129, v129, 1.0, v231
	v_med3_f32 v130, v130, 1.0, v231
	v_med3_f32 v131, v131, 1.0, v231
	v_med3_f32 v124, v124, 1.0, v231
	v_med3_f32 v125, v125, 1.0, v231
	v_med3_f32 v126, v126, 1.0, v231
	v_med3_f32 v127, v127, 1.0, v231
	v_med3_f32 v120, v120, 1.0, v231
	v_med3_f32 v121, v121, 1.0, v231
	v_med3_f32 v122, v122, 1.0, v231
	v_med3_f32 v123, v123, 1.0, v231
	v_med3_f32 v116, v116, 1.0, v231
	v_med3_f32 v117, v117, 1.0, v231
	v_med3_f32 v118, v118, 1.0, v231
	v_med3_f32 v119, v119, 1.0, v231
	v_cvt_u32_f32_e32 v128, v128
	v_cvt_u32_f32_e32 v120, v120
	v_cvt_u32_f32_sdwa v128, v129 dst_sel:BYTE_1 dst_unused:UNUSED_PRESERVE src0_sel:DWORD
	v_cvt_u32_f32_sdwa v120, v121 dst_sel:BYTE_1 dst_unused:UNUSED_PRESERVE src0_sel:DWORD
	v_cvt_u32_f32_e32 v129, v124
	v_cvt_u32_f32_e32 v121, v116
	v_cvt_u32_f32_sdwa v128, v130 dst_sel:BYTE_2 dst_unused:UNUSED_PRESERVE src0_sel:DWORD
	v_cvt_u32_f32_sdwa v120, v122 dst_sel:BYTE_2 dst_unused:UNUSED_PRESERVE src0_sel:DWORD
	v_cvt_u32_f32_sdwa v129, v125 dst_sel:BYTE_1 dst_unused:UNUSED_PRESERVE src0_sel:DWORD
	v_cvt_u32_f32_sdwa v121, v117 dst_sel:BYTE_1 dst_unused:UNUSED_PRESERVE src0_sel:DWORD
	v_cvt_u32_f32_sdwa v128, v131 dst_sel:BYTE_3 dst_unused:UNUSED_PRESERVE src0_sel:DWORD
	v_cvt_u32_f32_sdwa v120, v123 dst_sel:BYTE_3 dst_unused:UNUSED_PRESERVE src0_sel:DWORD
	v_cvt_u32_f32_sdwa v129, v126 dst_sel:BYTE_2 dst_unused:UNUSED_PRESERVE src0_sel:DWORD
	v_cvt_u32_f32_sdwa v121, v118 dst_sel:BYTE_2 dst_unused:UNUSED_PRESERVE src0_sel:DWORD
; __device__ __forceinline__ float sigmoid_f(float x) { return __builtin_amdgcn_rcpf(1.0f + __builtin_amdgcn_exp2f(-1.4426950408889634f * x)); }
; template <int ACT> __device__ __forceinline__ float act_f(float v) {
;     if (ACT == 1) return v * sigmoid_f(v);
;     if (ACT == 2) { const float u2 = 1.5957691216057308f * (v + 0.044715f * v * v * v); return v * sigmoid_f(u2); }
;     if (ACT == 3) return sigmoid_f(v);
;     template <int ACT, int AUX> __device__ __forceinline__ void run(const f32x4 (&acc)[2][2][4][2], const Unit& uu, int wr, int wc, int fr, int fq) const {
;     ...
;             for (int m = 0; m < 4; ++m) { const int r = row0 + ai * HALF + m * 16; const float rs = rsv[ai * 4 + m];
;                 bf16_t* rowp = O + (size_t)r * cfg::NC + col0; float s1 = 0.f, s2 = 0.f;
; #pragma unroll
;                 for (int bj = 0; bj < 2; ++bj) { f32x4 v0 = acc[ai][bj][m][0] * rs, v1 = acc[ai][bj][m][1] * rs;
; #pragma unroll
;                     for (int j = 0; j < 4; ++j) { v0[j] = act_f<ACT>(v0[j]); v1[j] = act_f<ACT>(v1[j]); }
;                     if (AUX == 4) {
;                         unsigned q[8];
; #pragma unroll
;                         for (int j = 0; j < 4; ++j) { q[j] = (unsigned)fminf(fmaxf(fmaf(v0[j], 255.0f, 0.5f), 1.0f), 255.0f); q[4 + j] = (unsigned)fminf(fmaxf(fmaf(v1[j], 255.0f, 0.5f), 1.0f), 255.0f); }
;                         u32x2 w8; w8.x = q[0] | (q[1] << 8) | (q[2] << 16) | (q[3] << 24); w8.y = q[4] | (q[5] << 8) | (q[6] << 16) | (q[7] << 24);
;                         __builtin_nontemporal_store(w8, (u32x2*)(g8 + ((size_t)((u.pn - 52) >> 4) * cfg::MT + r) * cfg::DM + ((u.pn - 52) & 15) * BM + wc * 32 + 8 * fq + bj * HALF));
	v_cvt_u32_f32_sdwa v129, v127 dst_sel:BYTE_3 dst_unused:UNUSED_PRESERVE src0_sel:DWORD
	v_cvt_u32_f32_sdwa v121, v119 dst_sel:BYTE_3 dst_unused:UNUSED_PRESERVE src0_sel:DWORD
	s_nop 0
	global_store_dwordx2 v[148:149], v[128:129], off offset:-4096 nt
	global_store_dwordx2 v[148:149], v[120:121], off offset:-3584 nt
	v_pk_mul_f32 v[112:113], v[112:113], v[162:163] op_sel_hi:[1,0]
	v_pk_mul_f32 v[114:115], v[114:115], v[162:163] op_sel_hi:[1,0]
	v_pk_mul_f32 v[108:109], v[108:109], v[162:163] op_sel_hi:[1,0]
	v_pk_mul_f32 v[110:111], v[110:111], v[162:163] op_sel_hi:[1,0]
	v_pk_mul_f32 v[104:105], v[104:105], v[162:163] op_sel_hi:[1,0]
	v_pk_mul_f32 v[106:107], v[106:107], v[162:163] op_sel_hi:[1,0]
	v_pk_mul_f32 v[100:101], v[100:101], v[162:163] op_sel_hi:[1,0]
	v_pk_mul_f32 v[102:103], v[102:103], v[162:163] op_sel_hi:[1,0]
	v_fmamk_f32 v164, v157, 0x39800000, v221
	v_rsq_f32_e32 v164, v164
	v_exp_f32_e32 v112, v112
	v_exp_f32_e32 v113, v113
	v_exp_f32_e32 v114, v114
	v_exp_f32_e32 v115, v115
	v_mul_f32_e32 v164, 0xbfb8aa3b, v164
	v_exp_f32_e32 v108, v108
	v_exp_f32_e32 v109, v109
	v_exp_f32_e32 v110, v110
	v_exp_f32_e32 v111, v111
	v_exp_f32_e32 v104, v104
	v_exp_f32_e32 v105, v105
	v_exp_f32_e32 v106, v106
	v_exp_f32_e32 v107, v107
	v_exp_f32_e32 v100, v100
	v_exp_f32_e32 v101, v101
	v_exp_f32_e32 v102, v102
	v_exp_f32_e32 v103, v103
	v_pk_add_f32 v[112:113], v[112:113], v[146:147] op_sel_hi:[1,0]
	v_pk_add_f32 v[114:115], v[114:115], v[146:147] op_sel_hi:[1,0]
	v_pk_add_f32 v[108:109], v[108:109], v[146:147] op_sel_hi:[1,0]
	v_pk_add_f32 v[110:111], v[110:111], v[146:147] op_sel_hi:[1,0]
	v_pk_add_f32 v[104:105], v[104:105], v[146:147] op_sel_hi:[1,0]
	v_pk_add_f32 v[106:107], v[106:107], v[146:147] op_sel_hi:[1,0]
	v_pk_add_f32 v[100:101], v[100:101], v[146:147] op_sel_hi:[1,0]
	v_pk_add_f32 v[102:103], v[102:103], v[146:147] op_sel_hi:[1,0]
	v_rcp_f32_e32 v112, v112
	v_rcp_f32_e32 v113, v113
	v_rcp_f32_e32 v114, v114
	v_rcp_f32_e32 v115, v115
	v_rcp_f32_e32 v108, v108
	v_rcp_f32_e32 v109, v109
	v_rcp_f32_e32 v110, v110
	v_rcp_f32_e32 v111, v111
	v_rcp_f32_e32 v104, v104
	v_rcp_f32_e32 v105, v105
	v_rcp_f32_e32 v106, v106
	v_rcp_f32_e32 v107, v107
	v_rcp_f32_e32 v100, v100
	v_rcp_f32_e32 v101, v101
	v_rcp_f32_e32 v102, v102
	v_rcp_f32_e32 v103, v103
	v_pk_fma_f32 v[112:113], v[112:113], v[150:151], v[152:153] op_sel_hi:[1,0,0]
	v_pk_fma_f32 v[114:115], v[114:115], v[150:151], v[152:153] op_sel_hi:[1,0,0]
	v_pk_fma_f32 v[108:109], v[108:109], v[150:151], v[152:153] op_sel_hi:[1,0,0]
	v_pk_fma_f32 v[110:111], v[110:111], v[150:151], v[152:153] op_sel_hi:[1,0,0]
	v_pk_fma_f32 v[104:105], v[104:105], v[150:151], v[152:153] op_sel_hi:[1,0,0]
	v_pk_fma_f32 v[106:107], v[106:107], v[150:151], v[152:153] op_sel_hi:[1,0,0]
	v_pk_fma_f32 v[100:101], v[100:101], v[150:151], v[152:153] op_sel_hi:[1,0,0]
	v_pk_fma_f32 v[102:103], v[102:103], v[150:151], v[152:153] op_sel_hi:[1,0,0]
	v_med3_f32 v112, v112, 1.0, v231
	v_med3_f32 v113, v113, 1.0, v231
	v_med3_f32 v114, v114, 1.0, v231
	v_med3_f32 v115, v115, 1.0, v231
	v_med3_f32 v108, v108, 1.0, v231
	v_med3_f32 v109, v109, 1.0, v231
	v_med3_f32 v110, v110, 1.0, v231
	v_med3_f32 v111, v111, 1.0, v231
	v_med3_f32 v104, v104, 1.0, v231
	v_med3_f32 v105, v105, 1.0, v231
	v_med3_f32 v106, v106, 1.0, v231
	v_med3_f32 v107, v107, 1.0, v231
	v_med3_f32 v100, v100, 1.0, v231
	v_med3_f32 v101, v101, 1.0, v231
	v_med3_f32 v102, v102, 1.0, v231
	v_med3_f32 v103, v103, 1.0, v231
	v_cvt_u32_f32_e32 v112, v112
	v_cvt_u32_f32_e32 v104, v104
	v_cvt_u32_f32_sdwa v112, v113 dst_sel:BYTE_1 dst_unused:UNUSED_PRESERVE src0_sel:DWORD
	v_cvt_u32_f32_sdwa v104, v105 dst_sel:BYTE_1 dst_unused:UNUSED_PRESERVE src0_sel:DWORD
	v_cvt_u32_f32_e32 v113, v108
	v_cvt_u32_f32_e32 v105, v100
	v_cvt_u32_f32_sdwa v112, v114 dst_sel:BYTE_2 dst_unused:UNUSED_PRESERVE src0_sel:DWORD
	v_cvt_u32_f32_sdwa v104, v106 dst_sel:BYTE_2 dst_unused:UNUSED_PRESERVE src0_sel:DWORD
	v_cvt_u32_f32_sdwa v113, v109 dst_sel:BYTE_1 dst_unused:UNUSED_PRESERVE src0_sel:DWORD
	v_cvt_u32_f32_sdwa v105, v101 dst_sel:BYTE_1 dst_unused:UNUSED_PRESERVE src0_sel:DWORD
	v_cvt_u32_f32_sdwa v112, v115 dst_sel:BYTE_3 dst_unused:UNUSED_PRESERVE src0_sel:DWORD
	v_cvt_u32_f32_sdwa v104, v107 dst_sel:BYTE_3 dst_unused:UNUSED_PRESERVE src0_sel:DWORD
	v_cvt_u32_f32_sdwa v113, v110 dst_sel:BYTE_2 dst_unused:UNUSED_PRESERVE src0_sel:DWORD
	v_cvt_u32_f32_sdwa v105, v102 dst_sel:BYTE_2 dst_unused:UNUSED_PRESERVE src0_sel:DWORD
	v_cvt_u32_f32_sdwa v113, v111 dst_sel:BYTE_3 dst_unused:UNUSED_PRESERVE src0_sel:DWORD
	v_cvt_u32_f32_sdwa v105, v103 dst_sel:BYTE_3 dst_unused:UNUSED_PRESERVE src0_sel:DWORD
	s_nop 0
	global_store_dwordx2 v[148:149], v[112:113], off offset:-3072 nt
	global_store_dwordx2 v[148:149], v[104:105], off offset:-2560 nt
	v_pk_mul_f32 v[96:97], v[96:97], v[160:161] op_sel_hi:[1,0]
	v_pk_mul_f32 v[98:99], v[98:99], v[160:161] op_sel_hi:[1,0]
	v_pk_mul_f32 v[92:93], v[92:93], v[160:161] op_sel_hi:[1,0]
	v_pk_mul_f32 v[94:95], v[94:95], v[160:161] op_sel_hi:[1,0]
	v_pk_mul_f32 v[88:89], v[88:89], v[160:161] op_sel_hi:[1,0]
	v_pk_mul_f32 v[90:91], v[90:91], v[160:161] op_sel_hi:[1,0]
	v_pk_mul_f32 v[84:85], v[84:85], v[160:161] op_sel_hi:[1,0]
	v_pk_mul_f32 v[86:87], v[86:87], v[160:161] op_sel_hi:[1,0]
	v_fmamk_f32 v162, v159, 0x39800000, v221
	v_rsq_f32_e32 v162, v162
	v_exp_f32_e32 v96, v96
	v_exp_f32_e32 v97, v97
	v_exp_f32_e32 v98, v98
	v_exp_f32_e32 v99, v99
	v_mul_f32_e32 v162, 0xbfb8aa3b, v162
	v_exp_f32_e32 v92, v92
	v_exp_f32_e32 v93, v93
	v_exp_f32_e32 v94, v94
	v_exp_f32_e32 v95, v95
	v_exp_f32_e32 v88, v88
	v_exp_f32_e32 v89, v89
	v_exp_f32_e32 v90, v90
; __device__ __forceinline__ float sigmoid_f(float x) { return __builtin_amdgcn_rcpf(1.0f + __builtin_amdgcn_exp2f(-1.4426950408889634f * x)); }
; template <int ACT> __device__ __forceinline__ float act_f(float v) {
;     if (ACT == 1) return v * sigmoid_f(v);
;     if (ACT == 2) { const float u2 = 1.5957691216057308f * (v + 0.044715f * v * v * v); return v * sigmoid_f(u2); }
;     if (ACT == 3) return sigmoid_f(v);
;     template <int ACT, int AUX> __device__ __forceinline__ void run(const f32x4 (&acc)[2][2][4][2], const Unit& uu, int wr, int wc, int fr, int fq) const {
;     ...
;             for (int m = 0; m < 4; ++m) { const int r = row0 + ai * HALF + m * 16; const float rs = rsv[ai * 4 + m];
;                 bf16_t* rowp = O + (size_t)r * cfg::NC + col0; float s1 = 0.f, s2 = 0.f;
; #pragma unroll
;                 for (int bj = 0; bj < 2; ++bj) { f32x4 v0 = acc[ai][bj][m][0] * rs, v1 = acc[ai][bj][m][1] * rs;
; #pragma unroll
;                     for (int j = 0; j < 4; ++j) { v0[j] = act_f<ACT>(v0[j]); v1[j] = act_f<ACT>(v1[j]); }
;                     if (AUX == 4) {
;                         unsigned q[8];
; #pragma unroll
;                         for (int j = 0; j < 4; ++j) { q[j] = (unsigned)fminf(fmaxf(fmaf(v0[j], 255.0f, 0.5f), 1.0f), 255.0f); q[4 + j] = (unsigned)fminf(fmaxf(fmaf(v1[j], 255.0f, 0.5f), 1.0f), 255.0f); }
;                         u32x2 w8; w8.x = q[0] | (q[1] << 8) | (q[2] << 16) | (q[3] << 24); w8.y = q[4] | (q[5] << 8) | (q[6] << 16) | (q[7] << 24);
;                         __builtin_nontemporal_store(w8, (u32x2*)(g8 + ((size_t)((u.pn - 52) >> 4) * cfg::MT + r) * cfg::DM + ((u.pn - 52) & 15) * BM + wc * 32 + 8 * fq + bj * HALF));
	v_exp_f32_e32 v91, v91
	v_exp_f32_e32 v84, v84
	v_exp_f32_e32 v85, v85
	v_exp_f32_e32 v86, v86
	v_exp_f32_e32 v87, v87
	v_pk_add_f32 v[96:97], v[96:97], v[146:147] op_sel_hi:[1,0]
	v_pk_add_f32 v[98:99], v[98:99], v[146:147] op_sel_hi:[1,0]
	v_pk_add_f32 v[92:93], v[92:93], v[146:147] op_sel_hi:[1,0]
	v_pk_add_f32 v[94:95], v[94:95], v[146:147] op_sel_hi:[1,0]
	v_pk_add_f32 v[88:89], v[88:89], v[146:147] op_sel_hi:[1,0]
	v_pk_add_f32 v[90:91], v[90:91], v[146:147] op_sel_hi:[1,0]
	v_pk_add_f32 v[84:85], v[84:85], v[146:147] op_sel_hi:[1,0]
	v_pk_add_f32 v[86:87], v[86:87], v[146:147] op_sel_hi:[1,0]
	v_rcp_f32_e32 v96, v96
	v_rcp_f32_e32 v97, v97
	v_rcp_f32_e32 v98, v98
	v_rcp_f32_e32 v99, v99
	v_rcp_f32_e32 v92, v92
	v_rcp_f32_e32 v93, v93
	v_rcp_f32_e32 v94, v94
	v_rcp_f32_e32 v95, v95
	v_rcp_f32_e32 v88, v88
	v_rcp_f32_e32 v89, v89
	v_rcp_f32_e32 v90, v90
	v_rcp_f32_e32 v91, v91
	v_rcp_f32_e32 v84, v84
	v_rcp_f32_e32 v85, v85
	v_rcp_f32_e32 v86, v86
	v_rcp_f32_e32 v87, v87
	v_pk_fma_f32 v[96:97], v[96:97], v[150:151], v[152:153] op_sel_hi:[1,0,0]
	v_pk_fma_f32 v[98:99], v[98:99], v[150:151], v[152:153] op_sel_hi:[1,0,0]
	v_pk_fma_f32 v[92:93], v[92:93], v[150:151], v[152:153] op_sel_hi:[1,0,0]
	v_pk_fma_f32 v[94:95], v[94:95], v[150:151], v[152:153] op_sel_hi:[1,0,0]
	v_pk_fma_f32 v[88:89], v[88:89], v[150:151], v[152:153] op_sel_hi:[1,0,0]
	v_pk_fma_f32 v[90:91], v[90:91], v[150:151], v[152:153] op_sel_hi:[1,0,0]
	v_pk_fma_f32 v[84:85], v[84:85], v[150:151], v[152:153] op_sel_hi:[1,0,0]
	v_pk_fma_f32 v[86:87], v[86:87], v[150:151], v[152:153] op_sel_hi:[1,0,0]
	v_med3_f32 v96, v96, 1.0, v231
	v_med3_f32 v97, v97, 1.0, v231
	v_med3_f32 v98, v98, 1.0, v231
	v_med3_f32 v99, v99, 1.0, v231
	v_med3_f32 v92, v92, 1.0, v231
	v_med3_f32 v93, v93, 1.0, v231
	v_med3_f32 v94, v94, 1.0, v231
	v_med3_f32 v95, v95, 1.0, v231
	v_med3_f32 v88, v88, 1.0, v231
	v_med3_f32 v89, v89, 1.0, v231
	v_med3_f32 v90, v90, 1.0, v231
	v_med3_f32 v91, v91, 1.0, v231
	v_med3_f32 v84, v84, 1.0, v231
	v_med3_f32 v85, v85, 1.0, v231
	v_med3_f32 v86, v86, 1.0, v231
	v_med3_f32 v87, v87, 1.0, v231
	v_cvt_u32_f32_e32 v96, v96
	v_cvt_u32_f32_e32 v88, v88
	v_cvt_u32_f32_sdwa v96, v97 dst_sel:BYTE_1 dst_unused:UNUSED_PRESERVE src0_sel:DWORD
	v_cvt_u32_f32_sdwa v88, v89 dst_sel:BYTE_1 dst_unused:UNUSED_PRESERVE src0_sel:DWORD
	v_cvt_u32_f32_e32 v97, v92
	v_cvt_u32_f32_e32 v89, v84
	v_cvt_u32_f32_sdwa v96, v98 dst_sel:BYTE_2 dst_unused:UNUSED_PRESERVE src0_sel:DWORD
	v_cvt_u32_f32_sdwa v88, v90 dst_sel:BYTE_2 dst_unused:UNUSED_PRESERVE src0_sel:DWORD
	v_cvt_u32_f32_sdwa v97, v93 dst_sel:BYTE_1 dst_unused:UNUSED_PRESERVE src0_sel:DWORD
	v_cvt_u32_f32_sdwa v89, v85 dst_sel:BYTE_1 dst_unused:UNUSED_PRESERVE src0_sel:DWORD
	v_cvt_u32_f32_sdwa v96, v99 dst_sel:BYTE_3 dst_unused:UNUSED_PRESERVE src0_sel:DWORD
	v_cvt_u32_f32_sdwa v88, v91 dst_sel:BYTE_3 dst_unused:UNUSED_PRESERVE src0_sel:DWORD
	v_cvt_u32_f32_sdwa v97, v94 dst_sel:BYTE_2 dst_unused:UNUSED_PRESERVE src0_sel:DWORD
	v_cvt_u32_f32_sdwa v89, v86 dst_sel:BYTE_2 dst_unused:UNUSED_PRESERVE src0_sel:DWORD
	v_cvt_u32_f32_sdwa v97, v95 dst_sel:BYTE_3 dst_unused:UNUSED_PRESERVE src0_sel:DWORD
	v_cvt_u32_f32_sdwa v89, v87 dst_sel:BYTE_3 dst_unused:UNUSED_PRESERVE src0_sel:DWORD
	s_nop 0
	global_store_dwordx2 v[148:149], v[96:97], off offset:-2048 nt
	global_store_dwordx2 v[148:149], v[88:89], off offset:-1536 nt
	v_pk_mul_f32 v[80:81], v[80:81], v[164:165] op_sel_hi:[1,0]
	v_pk_mul_f32 v[82:83], v[82:83], v[164:165] op_sel_hi:[1,0]
	v_pk_mul_f32 v[76:77], v[76:77], v[164:165] op_sel_hi:[1,0]
	v_pk_mul_f32 v[78:79], v[78:79], v[164:165] op_sel_hi:[1,0]
	v_pk_mul_f32 v[72:73], v[72:73], v[164:165] op_sel_hi:[1,0]
	v_pk_mul_f32 v[74:75], v[74:75], v[164:165] op_sel_hi:[1,0]
	v_pk_mul_f32 v[68:69], v[68:69], v[164:165] op_sel_hi:[1,0]
	v_pk_mul_f32 v[70:71], v[70:71], v[164:165] op_sel_hi:[1,0]
	v_fmamk_f32 v160, v154, 0x39800000, v221
	v_rsq_f32_e32 v160, v160
	v_exp_f32_e32 v80, v80
	v_exp_f32_e32 v81, v81
	v_exp_f32_e32 v82, v82
	v_exp_f32_e32 v83, v83
	v_mul_f32_e32 v160, 0xbfb8aa3b, v160
	v_exp_f32_e32 v76, v76
	v_exp_f32_e32 v77, v77
	v_exp_f32_e32 v78, v78
	v_exp_f32_e32 v79, v79
	v_exp_f32_e32 v72, v72
	v_exp_f32_e32 v73, v73
	v_exp_f32_e32 v74, v74
	v_exp_f32_e32 v75, v75
	v_exp_f32_e32 v68, v68
	v_exp_f32_e32 v69, v69
	v_exp_f32_e32 v70, v70
	v_exp_f32_e32 v71, v71
	v_pk_add_f32 v[80:81], v[80:81], v[146:147] op_sel_hi:[1,0]
	v_pk_add_f32 v[82:83], v[82:83], v[146:147] op_sel_hi:[1,0]
	v_pk_add_f32 v[76:77], v[76:77], v[146:147] op_sel_hi:[1,0]
	v_pk_add_f32 v[78:79], v[78:79], v[146:147] op_sel_hi:[1,0]
	v_pk_add_f32 v[72:73], v[72:73], v[146:147] op_sel_hi:[1,0]
	v_pk_add_f32 v[74:75], v[74:75], v[146:147] op_sel_hi:[1,0]
	v_pk_add_f32 v[68:69], v[68:69], v[146:147] op_sel_hi:[1,0]
	v_pk_add_f32 v[70:71], v[70:71], v[146:147] op_sel_hi:[1,0]
	v_rcp_f32_e32 v80, v80
	v_rcp_f32_e32 v81, v81
	v_rcp_f32_e32 v82, v82
	v_rcp_f32_e32 v83, v83
	v_rcp_f32_e32 v76, v76
	v_rcp_f32_e32 v77, v77
	v_rcp_f32_e32 v78, v78
	v_rcp_f32_e32 v79, v79
	v_rcp_f32_e32 v72, v72
	v_rcp_f32_e32 v73, v73
	v_rcp_f32_e32 v74, v74
	v_rcp_f32_e32 v75, v75
	v_rcp_f32_e32 v68, v68
	v_rcp_f32_e32 v69, v69
	v_rcp_f32_e32 v70, v70
	v_rcp_f32_e32 v71, v71
	v_pk_fma_f32 v[80:81], v[80:81], v[150:151], v[152:153] op_sel_hi:[1,0,0]
	v_pk_fma_f32 v[82:83], v[82:83], v[150:151], v[152:153] op_sel_hi:[1,0,0]
	v_pk_fma_f32 v[76:77], v[76:77], v[150:151], v[152:153] op_sel_hi:[1,0,0]
	v_pk_fma_f32 v[78:79], v[78:79], v[150:151], v[152:153] op_sel_hi:[1,0,0]
	v_pk_fma_f32 v[72:73], v[72:73], v[150:151], v[152:153] op_sel_hi:[1,0,0]
; __device__ __forceinline__ float sigmoid_f(float x) { return __builtin_amdgcn_rcpf(1.0f + __builtin_amdgcn_exp2f(-1.4426950408889634f * x)); }
; template <int ACT> __device__ __forceinline__ float act_f(float v) {
;     if (ACT == 1) return v * sigmoid_f(v);
;     if (ACT == 2) { const float u2 = 1.5957691216057308f * (v + 0.044715f * v * v * v); return v * sigmoid_f(u2); }
;     if (ACT == 3) return sigmoid_f(v);
;     template <int ACT, int AUX> __device__ __forceinline__ void run(const f32x4 (&acc)[2][2][4][2], const Unit& uu, int wr, int wc, int fr, int fq) const {
;     ...
;             for (int m = 0; m < 4; ++m) { const int r = row0 + ai * HALF + m * 16; const float rs = rsv[ai * 4 + m];
;                 bf16_t* rowp = O + (size_t)r * cfg::NC + col0; float s1 = 0.f, s2 = 0.f;
; #pragma unroll
;                 for (int bj = 0; bj < 2; ++bj) { f32x4 v0 = acc[ai][bj][m][0] * rs, v1 = acc[ai][bj][m][1] * rs;
; #pragma unroll
;                     for (int j = 0; j < 4; ++j) { v0[j] = act_f<ACT>(v0[j]); v1[j] = act_f<ACT>(v1[j]); }
;                     if (AUX == 4) {
;                         unsigned q[8];
; #pragma unroll
;                         for (int j = 0; j < 4; ++j) { q[j] = (unsigned)fminf(fmaxf(fmaf(v0[j], 255.0f, 0.5f), 1.0f), 255.0f); q[4 + j] = (unsigned)fminf(fmaxf(fmaf(v1[j], 255.0f, 0.5f), 1.0f), 255.0f); }
;                         u32x2 w8; w8.x = q[0] | (q[1] << 8) | (q[2] << 16) | (q[3] << 24); w8.y = q[4] | (q[5] << 8) | (q[6] << 16) | (q[7] << 24);
;                         __builtin_nontemporal_store(w8, (u32x2*)(g8 + ((size_t)((u.pn - 52) >> 4) * cfg::MT + r) * cfg::DM + ((u.pn - 52) & 15) * BM + wc * 32 + 8 * fq + bj * HALF));
	v_pk_fma_f32 v[74:75], v[74:75], v[150:151], v[152:153] op_sel_hi:[1,0,0]
	v_pk_fma_f32 v[68:69], v[68:69], v[150:151], v[152:153] op_sel_hi:[1,0,0]
	v_pk_fma_f32 v[70:71], v[70:71], v[150:151], v[152:153] op_sel_hi:[1,0,0]
	v_med3_f32 v80, v80, 1.0, v231
	v_med3_f32 v81, v81, 1.0, v231
	v_med3_f32 v82, v82, 1.0, v231
	v_med3_f32 v83, v83, 1.0, v231
	v_med3_f32 v76, v76, 1.0, v231
	v_med3_f32 v77, v77, 1.0, v231
	v_med3_f32 v78, v78, 1.0, v231
	v_med3_f32 v79, v79, 1.0, v231
	v_med3_f32 v72, v72, 1.0, v231
	v_med3_f32 v73, v73, 1.0, v231
	v_med3_f32 v74, v74, 1.0, v231
	v_med3_f32 v75, v75, 1.0, v231
	v_med3_f32 v68, v68, 1.0, v231
	v_med3_f32 v69, v69, 1.0, v231
	v_med3_f32 v70, v70, 1.0, v231
	v_med3_f32 v71, v71, 1.0, v231
	v_cvt_u32_f32_e32 v80, v80
	v_cvt_u32_f32_e32 v72, v72
	v_cvt_u32_f32_sdwa v80, v81 dst_sel:BYTE_1 dst_unused:UNUSED_PRESERVE src0_sel:DWORD
	v_cvt_u32_f32_sdwa v72, v73 dst_sel:BYTE_1 dst_unused:UNUSED_PRESERVE src0_sel:DWORD
	v_cvt_u32_f32_e32 v81, v76
	v_cvt_u32_f32_e32 v73, v68
	v_cvt_u32_f32_sdwa v80, v82 dst_sel:BYTE_2 dst_unused:UNUSED_PRESERVE src0_sel:DWORD
	v_cvt_u32_f32_sdwa v72, v74 dst_sel:BYTE_2 dst_unused:UNUSED_PRESERVE src0_sel:DWORD
	v_cvt_u32_f32_sdwa v81, v77 dst_sel:BYTE_1 dst_unused:UNUSED_PRESERVE src0_sel:DWORD
	v_cvt_u32_f32_sdwa v73, v69 dst_sel:BYTE_1 dst_unused:UNUSED_PRESERVE src0_sel:DWORD
	v_cvt_u32_f32_sdwa v80, v83 dst_sel:BYTE_3 dst_unused:UNUSED_PRESERVE src0_sel:DWORD
	v_cvt_u32_f32_sdwa v72, v75 dst_sel:BYTE_3 dst_unused:UNUSED_PRESERVE src0_sel:DWORD
	v_cvt_u32_f32_sdwa v81, v78 dst_sel:BYTE_2 dst_unused:UNUSED_PRESERVE src0_sel:DWORD
	v_cvt_u32_f32_sdwa v73, v70 dst_sel:BYTE_2 dst_unused:UNUSED_PRESERVE src0_sel:DWORD
	v_cvt_u32_f32_sdwa v81, v79 dst_sel:BYTE_3 dst_unused:UNUSED_PRESERVE src0_sel:DWORD
	v_cvt_u32_f32_sdwa v73, v71 dst_sel:BYTE_3 dst_unused:UNUSED_PRESERVE src0_sel:DWORD
	s_nop 0
	global_store_dwordx2 v[148:149], v[80:81], off offset:-1024 nt
	global_store_dwordx2 v[148:149], v[72:73], off offset:-512 nt
	v_pk_mul_f32 v[64:65], v[64:65], v[162:163] op_sel_hi:[1,0]
	v_pk_mul_f32 v[66:67], v[66:67], v[162:163] op_sel_hi:[1,0]
	v_pk_mul_f32 v[60:61], v[60:61], v[162:163] op_sel_hi:[1,0]
	v_pk_mul_f32 v[62:63], v[62:63], v[162:163] op_sel_hi:[1,0]
	v_pk_mul_f32 v[56:57], v[56:57], v[162:163] op_sel_hi:[1,0]
	v_pk_mul_f32 v[58:59], v[58:59], v[162:163] op_sel_hi:[1,0]
	v_pk_mul_f32 v[52:53], v[52:53], v[162:163] op_sel_hi:[1,0]
	v_pk_mul_f32 v[54:55], v[54:55], v[162:163] op_sel_hi:[1,0]
	v_fmamk_f32 v164, v156, 0x39800000, v221
	v_rsq_f32_e32 v164, v164
	v_exp_f32_e32 v64, v64
	v_exp_f32_e32 v65, v65
	v_exp_f32_e32 v66, v66
	v_exp_f32_e32 v67, v67
	v_mul_f32_e32 v164, 0xbfb8aa3b, v164
	v_exp_f32_e32 v60, v60
	v_exp_f32_e32 v61, v61
	v_exp_f32_e32 v62, v62
	v_exp_f32_e32 v63, v63
	v_exp_f32_e32 v56, v56
	v_exp_f32_e32 v57, v57
	v_exp_f32_e32 v58, v58
	v_exp_f32_e32 v59, v59
	v_exp_f32_e32 v52, v52
	v_exp_f32_e32 v53, v53
	v_exp_f32_e32 v54, v54
	v_exp_f32_e32 v55, v55
	v_pk_add_f32 v[64:65], v[64:65], v[146:147] op_sel_hi:[1,0]
	v_pk_add_f32 v[66:67], v[66:67], v[146:147] op_sel_hi:[1,0]
	v_pk_add_f32 v[60:61], v[60:61], v[146:147] op_sel_hi:[1,0]
	v_pk_add_f32 v[62:63], v[62:63], v[146:147] op_sel_hi:[1,0]
	v_pk_add_f32 v[56:57], v[56:57], v[146:147] op_sel_hi:[1,0]
	v_pk_add_f32 v[58:59], v[58:59], v[146:147] op_sel_hi:[1,0]
	v_pk_add_f32 v[52:53], v[52:53], v[146:147] op_sel_hi:[1,0]
	v_pk_add_f32 v[54:55], v[54:55], v[146:147] op_sel_hi:[1,0]
	v_rcp_f32_e32 v64, v64
	v_rcp_f32_e32 v65, v65
	v_rcp_f32_e32 v66, v66
	v_rcp_f32_e32 v67, v67
	v_rcp_f32_e32 v60, v60
	v_rcp_f32_e32 v61, v61
	v_rcp_f32_e32 v62, v62
	v_rcp_f32_e32 v63, v63
	v_rcp_f32_e32 v56, v56
	v_rcp_f32_e32 v57, v57
	v_rcp_f32_e32 v58, v58
	v_rcp_f32_e32 v59, v59
	v_rcp_f32_e32 v52, v52
	v_rcp_f32_e32 v53, v53
	v_rcp_f32_e32 v54, v54
	v_rcp_f32_e32 v55, v55
	v_pk_fma_f32 v[64:65], v[64:65], v[150:151], v[152:153] op_sel_hi:[1,0,0]
	v_pk_fma_f32 v[66:67], v[66:67], v[150:151], v[152:153] op_sel_hi:[1,0,0]
	v_pk_fma_f32 v[60:61], v[60:61], v[150:151], v[152:153] op_sel_hi:[1,0,0]
	v_pk_fma_f32 v[62:63], v[62:63], v[150:151], v[152:153] op_sel_hi:[1,0,0]
	v_pk_fma_f32 v[56:57], v[56:57], v[150:151], v[152:153] op_sel_hi:[1,0,0]
	v_pk_fma_f32 v[58:59], v[58:59], v[150:151], v[152:153] op_sel_hi:[1,0,0]
	v_pk_fma_f32 v[52:53], v[52:53], v[150:151], v[152:153] op_sel_hi:[1,0,0]
	v_pk_fma_f32 v[54:55], v[54:55], v[150:151], v[152:153] op_sel_hi:[1,0,0]
	v_med3_f32 v64, v64, 1.0, v231
	v_med3_f32 v65, v65, 1.0, v231
	v_med3_f32 v66, v66, 1.0, v231
	v_med3_f32 v67, v67, 1.0, v231
	v_med3_f32 v60, v60, 1.0, v231
	v_med3_f32 v61, v61, 1.0, v231
	v_med3_f32 v62, v62, 1.0, v231
	v_med3_f32 v63, v63, 1.0, v231
	v_med3_f32 v56, v56, 1.0, v231
	v_med3_f32 v57, v57, 1.0, v231
	v_med3_f32 v58, v58, 1.0, v231
	v_med3_f32 v59, v59, 1.0, v231
	v_med3_f32 v52, v52, 1.0, v231
	v_med3_f32 v53, v53, 1.0, v231
	v_med3_f32 v54, v54, 1.0, v231
	v_med3_f32 v55, v55, 1.0, v231
	v_cvt_u32_f32_e32 v64, v64
	v_cvt_u32_f32_e32 v56, v56
	v_cvt_u32_f32_sdwa v64, v65 dst_sel:BYTE_1 dst_unused:UNUSED_PRESERVE src0_sel:DWORD
	v_cvt_u32_f32_sdwa v56, v57 dst_sel:BYTE_1 dst_unused:UNUSED_PRESERVE src0_sel:DWORD
	v_cvt_u32_f32_e32 v65, v60
	v_cvt_u32_f32_e32 v57, v52
	v_cvt_u32_f32_sdwa v64, v66 dst_sel:BYTE_2 dst_unused:UNUSED_PRESERVE src0_sel:DWORD
	v_cvt_u32_f32_sdwa v56, v58 dst_sel:BYTE_2 dst_unused:UNUSED_PRESERVE src0_sel:DWORD
	v_cvt_u32_f32_sdwa v65, v61 dst_sel:BYTE_1 dst_unused:UNUSED_PRESERVE src0_sel:DWORD
	v_cvt_u32_f32_sdwa v57, v53 dst_sel:BYTE_1 dst_unused:UNUSED_PRESERVE src0_sel:DWORD
; __device__ __forceinline__ float sigmoid_f(float x) { return __builtin_amdgcn_rcpf(1.0f + __builtin_amdgcn_exp2f(-1.4426950408889634f * x)); }
; template <int ACT> __device__ __forceinline__ float act_f(float v) {
;     if (ACT == 1) return v * sigmoid_f(v);
;     if (ACT == 2) { const float u2 = 1.5957691216057308f * (v + 0.044715f * v * v * v); return v * sigmoid_f(u2); }
;     if (ACT == 3) return sigmoid_f(v);
;     template <int ACT, int AUX> __device__ __forceinline__ void run(const f32x4 (&acc)[2][2][4][2], const Unit& uu, int wr, int wc, int fr, int fq) const {
;     ...
;             for (int m = 0; m < 4; ++m) { const int r = row0 + ai * HALF + m * 16; const float rs = rsv[ai * 4 + m];
;                 bf16_t* rowp = O + (size_t)r * cfg::NC + col0; float s1 = 0.f, s2 = 0.f;
; #pragma unroll
;                 for (int bj = 0; bj < 2; ++bj) { f32x4 v0 = acc[ai][bj][m][0] * rs, v1 = acc[ai][bj][m][1] * rs;
; #pragma unroll
;                     for (int j = 0; j < 4; ++j) { v0[j] = act_f<ACT>(v0[j]); v1[j] = act_f<ACT>(v1[j]); }
;                     if (AUX == 4) {
;                         unsigned q[8];
; #pragma unroll
;                         for (int j = 0; j < 4; ++j) { q[j] = (unsigned)fminf(fmaxf(fmaf(v0[j], 255.0f, 0.5f), 1.0f), 255.0f); q[4 + j] = (unsigned)fminf(fmaxf(fmaf(v1[j], 255.0f, 0.5f), 1.0f), 255.0f); }
;                         u32x2 w8; w8.x = q[0] | (q[1] << 8) | (q[2] << 16) | (q[3] << 24); w8.y = q[4] | (q[5] << 8) | (q[6] << 16) | (q[7] << 24);
;                         __builtin_nontemporal_store(w8, (u32x2*)(g8 + ((size_t)((u.pn - 52) >> 4) * cfg::MT + r) * cfg::DM + ((u.pn - 52) & 15) * BM + wc * 32 + 8 * fq + bj * HALF));
	v_cvt_u32_f32_sdwa v64, v67 dst_sel:BYTE_3 dst_unused:UNUSED_PRESERVE src0_sel:DWORD
	v_cvt_u32_f32_sdwa v56, v59 dst_sel:BYTE_3 dst_unused:UNUSED_PRESERVE src0_sel:DWORD
	v_cvt_u32_f32_sdwa v65, v62 dst_sel:BYTE_2 dst_unused:UNUSED_PRESERVE src0_sel:DWORD
	v_cvt_u32_f32_sdwa v57, v54 dst_sel:BYTE_2 dst_unused:UNUSED_PRESERVE src0_sel:DWORD
	v_cvt_u32_f32_sdwa v65, v63 dst_sel:BYTE_3 dst_unused:UNUSED_PRESERVE src0_sel:DWORD
	v_cvt_u32_f32_sdwa v57, v55 dst_sel:BYTE_3 dst_unused:UNUSED_PRESERVE src0_sel:DWORD
	s_nop 0
	global_store_dwordx2 v[148:149], v[64:65], off offset:0 nt
	global_store_dwordx2 v[148:149], v[56:57], off offset:512 nt
	v_pk_mul_f32 v[48:49], v[48:49], v[160:161] op_sel_hi:[1,0]
	v_pk_mul_f32 v[50:51], v[50:51], v[160:161] op_sel_hi:[1,0]
	v_pk_mul_f32 v[44:45], v[44:45], v[160:161] op_sel_hi:[1,0]
	v_pk_mul_f32 v[46:47], v[46:47], v[160:161] op_sel_hi:[1,0]
	v_pk_mul_f32 v[40:41], v[40:41], v[160:161] op_sel_hi:[1,0]
	v_pk_mul_f32 v[42:43], v[42:43], v[160:161] op_sel_hi:[1,0]
	v_pk_mul_f32 v[36:37], v[36:37], v[160:161] op_sel_hi:[1,0]
	v_pk_mul_f32 v[38:39], v[38:39], v[160:161] op_sel_hi:[1,0]
	v_fmamk_f32 v162, v158, 0x39800000, v221
	v_rsq_f32_e32 v162, v162
	v_exp_f32_e32 v48, v48
	v_exp_f32_e32 v49, v49
	v_exp_f32_e32 v50, v50
	v_exp_f32_e32 v51, v51
	v_mul_f32_e32 v162, 0xbfb8aa3b, v162
	v_exp_f32_e32 v44, v44
	v_exp_f32_e32 v45, v45
	v_exp_f32_e32 v46, v46
	v_exp_f32_e32 v47, v47
	v_exp_f32_e32 v40, v40
	v_exp_f32_e32 v41, v41
	v_exp_f32_e32 v42, v42
	v_exp_f32_e32 v43, v43
	v_exp_f32_e32 v36, v36
	v_exp_f32_e32 v37, v37
	v_exp_f32_e32 v38, v38
	v_exp_f32_e32 v39, v39
	v_pk_add_f32 v[48:49], v[48:49], v[146:147] op_sel_hi:[1,0]
	v_pk_add_f32 v[50:51], v[50:51], v[146:147] op_sel_hi:[1,0]
	v_pk_add_f32 v[44:45], v[44:45], v[146:147] op_sel_hi:[1,0]
	v_pk_add_f32 v[46:47], v[46:47], v[146:147] op_sel_hi:[1,0]
	v_pk_add_f32 v[40:41], v[40:41], v[146:147] op_sel_hi:[1,0]
	v_pk_add_f32 v[42:43], v[42:43], v[146:147] op_sel_hi:[1,0]
	v_pk_add_f32 v[36:37], v[36:37], v[146:147] op_sel_hi:[1,0]
	v_pk_add_f32 v[38:39], v[38:39], v[146:147] op_sel_hi:[1,0]
	v_rcp_f32_e32 v48, v48
	v_rcp_f32_e32 v49, v49
	v_rcp_f32_e32 v50, v50
	v_rcp_f32_e32 v51, v51
	v_rcp_f32_e32 v44, v44
	v_rcp_f32_e32 v45, v45
	v_rcp_f32_e32 v46, v46
	v_rcp_f32_e32 v47, v47
	v_rcp_f32_e32 v40, v40
	v_rcp_f32_e32 v41, v41
	v_rcp_f32_e32 v42, v42
	v_rcp_f32_e32 v43, v43
	v_rcp_f32_e32 v36, v36
	v_rcp_f32_e32 v37, v37
	v_rcp_f32_e32 v38, v38
	v_rcp_f32_e32 v39, v39
	v_pk_fma_f32 v[48:49], v[48:49], v[150:151], v[152:153] op_sel_hi:[1,0,0]
	v_pk_fma_f32 v[50:51], v[50:51], v[150:151], v[152:153] op_sel_hi:[1,0,0]
	v_pk_fma_f32 v[44:45], v[44:45], v[150:151], v[152:153] op_sel_hi:[1,0,0]
	v_pk_fma_f32 v[46:47], v[46:47], v[150:151], v[152:153] op_sel_hi:[1,0,0]
	v_pk_fma_f32 v[40:41], v[40:41], v[150:151], v[152:153] op_sel_hi:[1,0,0]
	v_pk_fma_f32 v[42:43], v[42:43], v[150:151], v[152:153] op_sel_hi:[1,0,0]
	v_pk_fma_f32 v[36:37], v[36:37], v[150:151], v[152:153] op_sel_hi:[1,0,0]
	v_pk_fma_f32 v[38:39], v[38:39], v[150:151], v[152:153] op_sel_hi:[1,0,0]
	v_med3_f32 v48, v48, 1.0, v231
	v_med3_f32 v49, v49, 1.0, v231
	v_med3_f32 v50, v50, 1.0, v231
	v_med3_f32 v51, v51, 1.0, v231
	v_med3_f32 v44, v44, 1.0, v231
	v_med3_f32 v45, v45, 1.0, v231
	v_med3_f32 v46, v46, 1.0, v231
	v_med3_f32 v47, v47, 1.0, v231
	v_med3_f32 v40, v40, 1.0, v231
	v_med3_f32 v41, v41, 1.0, v231
	v_med3_f32 v42, v42, 1.0, v231
	v_med3_f32 v43, v43, 1.0, v231
	v_med3_f32 v36, v36, 1.0, v231
	v_med3_f32 v37, v37, 1.0, v231
	v_med3_f32 v38, v38, 1.0, v231
	v_med3_f32 v39, v39, 1.0, v231
	v_cvt_u32_f32_e32 v48, v48
	v_cvt_u32_f32_e32 v40, v40
	v_cvt_u32_f32_sdwa v48, v49 dst_sel:BYTE_1 dst_unused:UNUSED_PRESERVE src0_sel:DWORD
	v_cvt_u32_f32_sdwa v40, v41 dst_sel:BYTE_1 dst_unused:UNUSED_PRESERVE src0_sel:DWORD
	v_cvt_u32_f32_e32 v49, v44
	v_cvt_u32_f32_e32 v41, v36
	v_cvt_u32_f32_sdwa v48, v50 dst_sel:BYTE_2 dst_unused:UNUSED_PRESERVE src0_sel:DWORD
	v_cvt_u32_f32_sdwa v40, v42 dst_sel:BYTE_2 dst_unused:UNUSED_PRESERVE src0_sel:DWORD
	v_cvt_u32_f32_sdwa v49, v45 dst_sel:BYTE_1 dst_unused:UNUSED_PRESERVE src0_sel:DWORD
	v_cvt_u32_f32_sdwa v41, v37 dst_sel:BYTE_1 dst_unused:UNUSED_PRESERVE src0_sel:DWORD
	v_cvt_u32_f32_sdwa v48, v51 dst_sel:BYTE_3 dst_unused:UNUSED_PRESERVE src0_sel:DWORD
	v_cvt_u32_f32_sdwa v40, v43 dst_sel:BYTE_3 dst_unused:UNUSED_PRESERVE src0_sel:DWORD
	v_cvt_u32_f32_sdwa v49, v46 dst_sel:BYTE_2 dst_unused:UNUSED_PRESERVE src0_sel:DWORD
	v_cvt_u32_f32_sdwa v41, v38 dst_sel:BYTE_2 dst_unused:UNUSED_PRESERVE src0_sel:DWORD
	v_cvt_u32_f32_sdwa v49, v47 dst_sel:BYTE_3 dst_unused:UNUSED_PRESERVE src0_sel:DWORD
	v_cvt_u32_f32_sdwa v41, v39 dst_sel:BYTE_3 dst_unused:UNUSED_PRESERVE src0_sel:DWORD
	s_nop 0
	global_store_dwordx2 v[148:149], v[48:49], off offset:1024 nt
	global_store_dwordx2 v[148:149], v[40:41], off offset:1536 nt
	v_pk_mul_f32 v[32:33], v[32:33], v[164:165] op_sel_hi:[1,0]
	v_pk_mul_f32 v[34:35], v[34:35], v[164:165] op_sel_hi:[1,0]
	v_pk_mul_f32 v[28:29], v[28:29], v[164:165] op_sel_hi:[1,0]
	v_pk_mul_f32 v[30:31], v[30:31], v[164:165] op_sel_hi:[1,0]
	v_pk_mul_f32 v[24:25], v[24:25], v[164:165] op_sel_hi:[1,0]
	v_pk_mul_f32 v[26:27], v[26:27], v[164:165] op_sel_hi:[1,0]
	v_pk_mul_f32 v[20:21], v[20:21], v[164:165] op_sel_hi:[1,0]
	v_pk_mul_f32 v[22:23], v[22:23], v[164:165] op_sel_hi:[1,0]
	v_exp_f32_e32 v32, v32
	v_exp_f32_e32 v33, v33
	v_exp_f32_e32 v34, v34
	v_exp_f32_e32 v35, v35
	v_exp_f32_e32 v28, v28
	v_exp_f32_e32 v29, v29
	v_exp_f32_e32 v30, v30
	v_exp_f32_e32 v31, v31
	v_exp_f32_e32 v24, v24
	v_exp_f32_e32 v25, v25
	v_exp_f32_e32 v26, v26
; __device__ __forceinline__ float sigmoid_f(float x) { return __builtin_amdgcn_rcpf(1.0f + __builtin_amdgcn_exp2f(-1.4426950408889634f * x)); }
; template <int ACT> __device__ __forceinline__ float act_f(float v) {
;     if (ACT == 1) return v * sigmoid_f(v);
;     if (ACT == 2) { const float u2 = 1.5957691216057308f * (v + 0.044715f * v * v * v); return v * sigmoid_f(u2); }
;     if (ACT == 3) return sigmoid_f(v);
;     template <int ACT, int AUX> __device__ __forceinline__ void run(const f32x4 (&acc)[2][2][4][2], const Unit& uu, int wr, int wc, int fr, int fq) const {
;     ...
;             for (int m = 0; m < 4; ++m) { const int r = row0 + ai * HALF + m * 16; const float rs = rsv[ai * 4 + m];
;                 bf16_t* rowp = O + (size_t)r * cfg::NC + col0; float s1 = 0.f, s2 = 0.f;
; #pragma unroll
;                 for (int bj = 0; bj < 2; ++bj) { f32x4 v0 = acc[ai][bj][m][0] * rs, v1 = acc[ai][bj][m][1] * rs;
; #pragma unroll
;                     for (int j = 0; j < 4; ++j) { v0[j] = act_f<ACT>(v0[j]); v1[j] = act_f<ACT>(v1[j]); }
;                     if (AUX == 4) {
;                         unsigned q[8];
; #pragma unroll
;                         for (int j = 0; j < 4; ++j) { q[j] = (unsigned)fminf(fmaxf(fmaf(v0[j], 255.0f, 0.5f), 1.0f), 255.0f); q[4 + j] = (unsigned)fminf(fmaxf(fmaf(v1[j], 255.0f, 0.5f), 1.0f), 255.0f); }
;                         u32x2 w8; w8.x = q[0] | (q[1] << 8) | (q[2] << 16) | (q[3] << 24); w8.y = q[4] | (q[5] << 8) | (q[6] << 16) | (q[7] << 24);
;                         __builtin_nontemporal_store(w8, (u32x2*)(g8 + ((size_t)((u.pn - 52) >> 4) * cfg::MT + r) * cfg::DM + ((u.pn - 52) & 15) * BM + wc * 32 + 8 * fq + bj * HALF));
	v_exp_f32_e32 v27, v27
	v_exp_f32_e32 v20, v20
	v_exp_f32_e32 v21, v21
	v_exp_f32_e32 v22, v22
	v_exp_f32_e32 v23, v23
	v_pk_add_f32 v[32:33], v[32:33], v[146:147] op_sel_hi:[1,0]
	v_pk_add_f32 v[34:35], v[34:35], v[146:147] op_sel_hi:[1,0]
	v_pk_add_f32 v[28:29], v[28:29], v[146:147] op_sel_hi:[1,0]
	v_pk_add_f32 v[30:31], v[30:31], v[146:147] op_sel_hi:[1,0]
	v_pk_add_f32 v[24:25], v[24:25], v[146:147] op_sel_hi:[1,0]
	v_pk_add_f32 v[26:27], v[26:27], v[146:147] op_sel_hi:[1,0]
	v_pk_add_f32 v[20:21], v[20:21], v[146:147] op_sel_hi:[1,0]
	v_pk_add_f32 v[22:23], v[22:23], v[146:147] op_sel_hi:[1,0]
	v_rcp_f32_e32 v32, v32
	v_rcp_f32_e32 v33, v33
	v_rcp_f32_e32 v34, v34
	v_rcp_f32_e32 v35, v35
	v_rcp_f32_e32 v28, v28
	v_rcp_f32_e32 v29, v29
	v_rcp_f32_e32 v30, v30
	v_rcp_f32_e32 v31, v31
	v_rcp_f32_e32 v24, v24
	v_rcp_f32_e32 v25, v25
	v_rcp_f32_e32 v26, v26
	v_rcp_f32_e32 v27, v27
	v_rcp_f32_e32 v20, v20
	v_rcp_f32_e32 v21, v21
	v_rcp_f32_e32 v22, v22
	v_rcp_f32_e32 v23, v23
	v_pk_fma_f32 v[32:33], v[32:33], v[150:151], v[152:153] op_sel_hi:[1,0,0]
	v_pk_fma_f32 v[34:35], v[34:35], v[150:151], v[152:153] op_sel_hi:[1,0,0]
	v_pk_fma_f32 v[28:29], v[28:29], v[150:151], v[152:153] op_sel_hi:[1,0,0]
	v_pk_fma_f32 v[30:31], v[30:31], v[150:151], v[152:153] op_sel_hi:[1,0,0]
	v_pk_fma_f32 v[24:25], v[24:25], v[150:151], v[152:153] op_sel_hi:[1,0,0]
	v_pk_fma_f32 v[26:27], v[26:27], v[150:151], v[152:153] op_sel_hi:[1,0,0]
	v_pk_fma_f32 v[20:21], v[20:21], v[150:151], v[152:153] op_sel_hi:[1,0,0]
	v_pk_fma_f32 v[22:23], v[22:23], v[150:151], v[152:153] op_sel_hi:[1,0,0]
	v_med3_f32 v32, v32, 1.0, v231
	v_med3_f32 v33, v33, 1.0, v231
	v_med3_f32 v34, v34, 1.0, v231
	v_med3_f32 v35, v35, 1.0, v231
	v_med3_f32 v28, v28, 1.0, v231
	v_med3_f32 v29, v29, 1.0, v231
	v_med3_f32 v30, v30, 1.0, v231
	v_med3_f32 v31, v31, 1.0, v231
	v_med3_f32 v24, v24, 1.0, v231
	v_med3_f32 v25, v25, 1.0, v231
	v_med3_f32 v26, v26, 1.0, v231
	v_med3_f32 v27, v27, 1.0, v231
	v_med3_f32 v20, v20, 1.0, v231
	v_med3_f32 v21, v21, 1.0, v231
	v_med3_f32 v22, v22, 1.0, v231
	v_med3_f32 v23, v23, 1.0, v231
	v_cvt_u32_f32_e32 v32, v32
	v_cvt_u32_f32_e32 v24, v24
	v_cvt_u32_f32_sdwa v32, v33 dst_sel:BYTE_1 dst_unused:UNUSED_PRESERVE src0_sel:DWORD
	v_cvt_u32_f32_sdwa v24, v25 dst_sel:BYTE_1 dst_unused:UNUSED_PRESERVE src0_sel:DWORD
	v_cvt_u32_f32_e32 v33, v28
	v_cvt_u32_f32_e32 v25, v20
	v_cvt_u32_f32_sdwa v32, v34 dst_sel:BYTE_2 dst_unused:UNUSED_PRESERVE src0_sel:DWORD
	v_cvt_u32_f32_sdwa v24, v26 dst_sel:BYTE_2 dst_unused:UNUSED_PRESERVE src0_sel:DWORD
	v_cvt_u32_f32_sdwa v33, v29 dst_sel:BYTE_1 dst_unused:UNUSED_PRESERVE src0_sel:DWORD
	v_cvt_u32_f32_sdwa v25, v21 dst_sel:BYTE_1 dst_unused:UNUSED_PRESERVE src0_sel:DWORD
	v_cvt_u32_f32_sdwa v32, v35 dst_sel:BYTE_3 dst_unused:UNUSED_PRESERVE src0_sel:DWORD
	v_cvt_u32_f32_sdwa v24, v27 dst_sel:BYTE_3 dst_unused:UNUSED_PRESERVE src0_sel:DWORD
	v_cvt_u32_f32_sdwa v33, v30 dst_sel:BYTE_2 dst_unused:UNUSED_PRESERVE src0_sel:DWORD
	v_cvt_u32_f32_sdwa v25, v22 dst_sel:BYTE_2 dst_unused:UNUSED_PRESERVE src0_sel:DWORD
	v_cvt_u32_f32_sdwa v33, v31 dst_sel:BYTE_3 dst_unused:UNUSED_PRESERVE src0_sel:DWORD
	v_cvt_u32_f32_sdwa v25, v23 dst_sel:BYTE_3 dst_unused:UNUSED_PRESERVE src0_sel:DWORD
	s_nop 0
	global_store_dwordx2 v[148:149], v[32:33], off offset:2048 nt
	global_store_dwordx2 v[148:149], v[24:25], off offset:2560 nt
	v_pk_mul_f32 v[16:17], v[16:17], v[162:163] op_sel_hi:[1,0]
	v_pk_mul_f32 v[18:19], v[18:19], v[162:163] op_sel_hi:[1,0]
	v_pk_mul_f32 v[12:13], v[12:13], v[162:163] op_sel_hi:[1,0]
	v_pk_mul_f32 v[14:15], v[14:15], v[162:163] op_sel_hi:[1,0]
	v_pk_mul_f32 v[8:9], v[8:9], v[162:163] op_sel_hi:[1,0]
	v_pk_mul_f32 v[10:11], v[10:11], v[162:163] op_sel_hi:[1,0]
; __device__ __forceinline__ float sigmoid_f(float x) { return __builtin_amdgcn_rcpf(1.0f + __builtin_amdgcn_exp2f(-1.4426950408889634f * x)); }
; template <int ACT> __device__ __forceinline__ float act_f(float v) {
;     if (ACT == 1) return v * sigmoid_f(v);
;     if (ACT == 2) { const float u2 = 1.5957691216057308f * (v + 0.044715f * v * v * v); return v * sigmoid_f(u2); }
;     if (ACT == 3) return sigmoid_f(v);
;     template <int ACT, int AUX> __device__ __forceinline__ void run(const f32x4 (&acc)[2][2][4][2], const Unit& uu, int wr, int wc, int fr, int fq) const {
;     ...
;             for (int m = 0; m < 4; ++m) { const int r = row0 + ai * HALF + m * 16; const float rs = rsv[ai * 4 + m];
;                 bf16_t* rowp = O + (size_t)r * cfg::NC + col0; float s1 = 0.f, s2 = 0.f;
; #pragma unroll
;                 for (int bj = 0; bj < 2; ++bj) { f32x4 v0 = acc[ai][bj][m][0] * rs, v1 = acc[ai][bj][m][1] * rs;
; #pragma unroll
;                     for (int j = 0; j < 4; ++j) { v0[j] = act_f<ACT>(v0[j]); v1[j] = act_f<ACT>(v1[j]); }
;                     if (AUX == 4) {
;                         unsigned q[8];
; #pragma unroll
;                         for (int j = 0; j < 4; ++j) { q[j] = (unsigned)fminf(fmaxf(fmaf(v0[j], 255.0f, 0.5f), 1.0f), 255.0f); q[4 + j] = (unsigned)fminf(fmaxf(fmaf(v1[j], 255.0f, 0.5f), 1.0f), 255.0f); }
;                         u32x2 w8; w8.x = q[0] | (q[1] << 8) | (q[2] << 16) | (q[3] << 24); w8.y = q[4] | (q[5] << 8) | (q[6] << 16) | (q[7] << 24);
;                         __builtin_nontemporal_store(w8, (u32x2*)(g8 + ((size_t)((u.pn - 52) >> 4) * cfg::MT + r) * cfg::DM + ((u.pn - 52) & 15) * BM + wc * 32 + 8 * fq + bj * HALF));
	v_pk_mul_f32 v[4:5], v[4:5], v[162:163] op_sel_hi:[1,0]
	v_pk_mul_f32 v[6:7], v[6:7], v[162:163] op_sel_hi:[1,0]
	v_exp_f32_e32 v16, v16
	v_exp_f32_e32 v17, v17
	v_exp_f32_e32 v18, v18
	v_exp_f32_e32 v19, v19
	v_exp_f32_e32 v12, v12
	v_exp_f32_e32 v13, v13
	v_exp_f32_e32 v14, v14
	v_exp_f32_e32 v15, v15
	v_exp_f32_e32 v8, v8
	v_exp_f32_e32 v9, v9
	v_exp_f32_e32 v10, v10
	v_exp_f32_e32 v11, v11
	v_exp_f32_e32 v4, v4
	v_exp_f32_e32 v5, v5
	v_exp_f32_e32 v6, v6
	v_exp_f32_e32 v7, v7
	v_pk_add_f32 v[16:17], v[16:17], v[146:147] op_sel_hi:[1,0]
	v_pk_add_f32 v[18:19], v[18:19], v[146:147] op_sel_hi:[1,0]
	v_pk_add_f32 v[12:13], v[12:13], v[146:147] op_sel_hi:[1,0]
	v_pk_add_f32 v[14:15], v[14:15], v[146:147] op_sel_hi:[1,0]
	v_pk_add_f32 v[8:9], v[8:9], v[146:147] op_sel_hi:[1,0]
	v_pk_add_f32 v[10:11], v[10:11], v[146:147] op_sel_hi:[1,0]
	v_pk_add_f32 v[4:5], v[4:5], v[146:147] op_sel_hi:[1,0]
	v_pk_add_f32 v[6:7], v[6:7], v[146:147] op_sel_hi:[1,0]
	v_rcp_f32_e32 v16, v16
	v_rcp_f32_e32 v17, v17
	v_rcp_f32_e32 v18, v18
	v_rcp_f32_e32 v19, v19
	v_rcp_f32_e32 v12, v12
	v_rcp_f32_e32 v13, v13
	v_rcp_f32_e32 v14, v14
	v_rcp_f32_e32 v15, v15
	v_rcp_f32_e32 v8, v8
	v_rcp_f32_e32 v9, v9
	v_rcp_f32_e32 v10, v10
	v_rcp_f32_e32 v11, v11
	v_rcp_f32_e32 v4, v4
	v_rcp_f32_e32 v5, v5
	v_rcp_f32_e32 v6, v6
	v_rcp_f32_e32 v7, v7
	v_pk_fma_f32 v[16:17], v[16:17], v[150:151], v[152:153] op_sel_hi:[1,0,0]
	v_pk_fma_f32 v[18:19], v[18:19], v[150:151], v[152:153] op_sel_hi:[1,0,0]
	v_pk_fma_f32 v[12:13], v[12:13], v[150:151], v[152:153] op_sel_hi:[1,0,0]
	v_pk_fma_f32 v[14:15], v[14:15], v[150:151], v[152:153] op_sel_hi:[1,0,0]
	v_pk_fma_f32 v[8:9], v[8:9], v[150:151], v[152:153] op_sel_hi:[1,0,0]
	v_pk_fma_f32 v[10:11], v[10:11], v[150:151], v[152:153] op_sel_hi:[1,0,0]
	v_pk_fma_f32 v[4:5], v[4:5], v[150:151], v[152:153] op_sel_hi:[1,0,0]
	v_pk_fma_f32 v[6:7], v[6:7], v[150:151], v[152:153] op_sel_hi:[1,0,0]
	v_med3_f32 v16, v16, 1.0, v231
	v_med3_f32 v17, v17, 1.0, v231
	v_med3_f32 v18, v18, 1.0, v231
	v_med3_f32 v19, v19, 1.0, v231
	v_med3_f32 v12, v12, 1.0, v231
	v_med3_f32 v13, v13, 1.0, v231
	v_med3_f32 v14, v14, 1.0, v231
	v_med3_f32 v15, v15, 1.0, v231
	v_med3_f32 v8, v8, 1.0, v231
	v_med3_f32 v9, v9, 1.0, v231
	v_med3_f32 v10, v10, 1.0, v231
	v_med3_f32 v11, v11, 1.0, v231
	v_med3_f32 v4, v4, 1.0, v231
	v_med3_f32 v5, v5, 1.0, v231
	v_med3_f32 v6, v6, 1.0, v231
	v_med3_f32 v7, v7, 1.0, v231
	v_cvt_u32_f32_e32 v16, v16
	v_cvt_u32_f32_e32 v8, v8
	v_cvt_u32_f32_sdwa v16, v17 dst_sel:BYTE_1 dst_unused:UNUSED_PRESERVE src0_sel:DWORD
	v_cvt_u32_f32_sdwa v8, v9 dst_sel:BYTE_1 dst_unused:UNUSED_PRESERVE src0_sel:DWORD
	v_cvt_u32_f32_e32 v17, v12
	v_cvt_u32_f32_e32 v9, v4
	v_cvt_u32_f32_sdwa v16, v18 dst_sel:BYTE_2 dst_unused:UNUSED_PRESERVE src0_sel:DWORD
	v_cvt_u32_f32_sdwa v8, v10 dst_sel:BYTE_2 dst_unused:UNUSED_PRESERVE src0_sel:DWORD
	v_cvt_u32_f32_sdwa v17, v13 dst_sel:BYTE_1 dst_unused:UNUSED_PRESERVE src0_sel:DWORD
	v_cvt_u32_f32_sdwa v9, v5 dst_sel:BYTE_1 dst_unused:UNUSED_PRESERVE src0_sel:DWORD
	v_cvt_u32_f32_sdwa v16, v19 dst_sel:BYTE_3 dst_unused:UNUSED_PRESERVE src0_sel:DWORD
	v_cvt_u32_f32_sdwa v8, v11 dst_sel:BYTE_3 dst_unused:UNUSED_PRESERVE src0_sel:DWORD
	v_cvt_u32_f32_sdwa v17, v14 dst_sel:BYTE_2 dst_unused:UNUSED_PRESERVE src0_sel:DWORD
	v_cvt_u32_f32_sdwa v9, v6 dst_sel:BYTE_2 dst_unused:UNUSED_PRESERVE src0_sel:DWORD
	v_cvt_u32_f32_sdwa v17, v15 dst_sel:BYTE_3 dst_unused:UNUSED_PRESERVE src0_sel:DWORD
	v_cvt_u32_f32_sdwa v9, v7 dst_sel:BYTE_3 dst_unused:UNUSED_PRESERVE src0_sel:DWORD
	s_nop 0
	global_store_dwordx2 v[148:149], v[16:17], off offset:3072 nt
	global_store_dwordx2 v[148:149], v[8:9], off offset:3584 nt
	s_mov_b32 s2, 0xb0000
	s_mov_b64 s[12:13], 0xb0000
